# speedup vs baseline: 1.0114x; 1.0004x over previous
.LBB2_18:
	s_or_b64 exec, exec, s[0:1]
	v_lshrrev_b32_e32 v1, 7, v0
	v_and_b32_e32 v2, 0x7f, v0
	v_lshlrev_b32_e32 v38, 2, v2
	s_mul_i32 s8, s22, 0x2ee
	s_mov_b64 s[0:1], 0x1000
	v_mul_u32_u24_e32 v3, 38, v1
	v_add_lshl_u32 v4, s8, v3, 9
	v_mov_b32_e32 v5, 0
	v_lshl_add_u64 v[40:41], s[16:17], 0, v[4:5]
	v_mov_b32_e32 v6, v38
	v_mov_b32_e32 v7, 0
	v_lshl_add_u64 v[40:41], v[40:41], 0, v[6:7]
	v_mul_u32_u24_e32 v3, 19, v1
	v_add_lshl_u32 v4, s8, v3, 9
	v_lshl_add_u64 v[42:43], s[4:5], 0, v[4:5]
	v_lshl_add_u64 v[42:43], v[42:43], 0, v[6:7]
	v_lshl_add_u64 v[44:45], s[6:7], 0, v[4:5]
	v_lshl_add_u64 v[44:45], v[44:45], 0, v[6:7]
	v_mul_u32_u24_e32 v39, 0x98, v1
	v_add_u32_e32 v39, 0xe800, v39
	v_add_u32_e32 v71, 0x980, v39
	global_load_dword v80, v[40:41], off
	global_load_dword v81, v[40:41], off offset:512
	global_load_dword v82, v[40:41], off offset:1024
	global_load_dword v83, v[40:41], off offset:1536
	global_load_dword v84, v[40:41], off offset:2048
	global_load_dword v85, v[40:41], off offset:2560
	global_load_dword v86, v[40:41], off offset:3072
	global_load_dword v87, v[40:41], off offset:3584
	v_lshl_add_u64 v[40:41], v[40:41], 0, s[0:1]
	global_load_dword v88, v[40:41], off
	global_load_dword v89, v[40:41], off offset:512
	global_load_dword v90, v[40:41], off offset:1024
	global_load_dword v91, v[40:41], off offset:1536
	global_load_dword v92, v[40:41], off offset:2048
	global_load_dword v93, v[40:41], off offset:2560
	global_load_dword v94, v[40:41], off offset:3072
	global_load_dword v95, v[40:41], off offset:3584
	v_lshl_add_u64 v[40:41], v[40:41], 0, s[0:1]
	global_load_dword v96, v[40:41], off
	global_load_dword v97, v[40:41], off offset:512
	global_load_dword v98, v[40:41], off offset:1024
	global_load_dword v99, v[40:41], off offset:1536
	global_load_dword v100, v[40:41], off offset:2048
	global_load_dword v101, v[40:41], off offset:2560
	global_load_dword v102, v[40:41], off offset:3072
	global_load_dword v103, v[40:41], off offset:3584
	v_lshl_add_u64 v[40:41], v[40:41], 0, s[0:1]
	global_load_dword v104, v[40:41], off
	global_load_dword v105, v[40:41], off offset:512
	global_load_dword v106, v[40:41], off offset:1024
	global_load_dword v107, v[40:41], off offset:1536
	global_load_dword v108, v[40:41], off offset:2048
	global_load_dword v109, v[40:41], off offset:2560
	global_load_dword v110, v[40:41], off offset:3072
	global_load_dword v111, v[40:41], off offset:3584
	v_lshl_add_u64 v[40:41], v[40:41], 0, s[0:1]
	global_load_dword v112, v[40:41], off
	global_load_dword v113, v[40:41], off offset:512
	global_load_dword v114, v[40:41], off offset:1024
	global_load_dword v115, v[40:41], off offset:1536
	global_load_dword v116, v[40:41], off offset:2048
	global_load_dword v117, v[40:41], off offset:2560
	global_load_dword v2, v[42:43], off
	global_load_dword v3, v[44:45], off
	global_load_dword v4, v[42:43], off offset:512
	global_load_dword v5, v[44:45], off offset:512
	global_load_dword v6, v[42:43], off offset:1024
	global_load_dword v7, v[44:45], off offset:1024
	global_load_dword v8, v[42:43], off offset:1536
	global_load_dword v9, v[44:45], off offset:1536
	global_load_dword v10, v[42:43], off offset:2048
	global_load_dword v11, v[44:45], off offset:2048
	global_load_dword v12, v[42:43], off offset:2560
	global_load_dword v13, v[44:45], off offset:2560
	global_load_dword v14, v[42:43], off offset:3072
	global_load_dword v15, v[44:45], off offset:3072
	global_load_dword v16, v[42:43], off offset:3584
	global_load_dword v17, v[44:45], off offset:3584
	v_lshl_add_u64 v[42:43], v[42:43], 0, s[0:1]
	v_lshl_add_u64 v[44:45], v[44:45], 0, s[0:1]
	global_load_dword v18, v[42:43], off
	global_load_dword v19, v[44:45], off
	global_load_dword v20, v[42:43], off offset:512
	global_load_dword v21, v[44:45], off offset:512
	global_load_dword v22, v[42:43], off offset:1024
	global_load_dword v23, v[44:45], off offset:1024
	global_load_dword v24, v[42:43], off offset:1536
	global_load_dword v25, v[44:45], off offset:1536
	global_load_dword v26, v[42:43], off offset:2048
	global_load_dword v27, v[44:45], off offset:2048
	global_load_dword v28, v[42:43], off offset:2560
	global_load_dword v29, v[44:45], off offset:2560
	global_load_dword v30, v[42:43], off offset:3072
	global_load_dword v31, v[44:45], off offset:3072
	global_load_dword v32, v[42:43], off offset:3584
	global_load_dword v33, v[44:45], off offset:3584
	v_lshl_add_u64 v[42:43], v[42:43], 0, s[0:1]
	v_lshl_add_u64 v[44:45], v[44:45], 0, s[0:1]
	global_load_dword v34, v[42:43], off
	global_load_dword v35, v[44:45], off
	global_load_dword v36, v[42:43], off offset:512
	global_load_dword v37, v[44:45], off offset:512
	global_load_dword v118, v[42:43], off offset:1024
	global_load_dword v119, v[44:45], off offset:1024
	v_mov_b32_e32 v76, 0
	v_mov_b32_e32 v77, 0
	v_mov_b32_e32 v78, 0
	v_mov_b32_e32 v79, 0
	v_mov_b32_e32 v120, 0
	v_mov_b32_e32 v121, 0
	v_mov_b32_e32 v122, 0
	v_mov_b32_e32 v123, 0
	s_waitcnt lgkmcnt(0)
	s_barrier
	ds_read2_b64 v[40:43], v39 offset0:0 offset1:1
	ds_read2_b64 v[44:47], v39 offset0:152 offset1:153
	ds_read2_b64 v[48:51], v71 offset0:0 offset1:1
	ds_read2_b64 v[52:55], v71 offset0:152 offset1:153
	ds_read2_b64 v[56:59], v39 offset0:2 offset1:3
	ds_read2_b64 v[60:63], v39 offset0:154 offset1:155
	ds_read2_b64 v[64:67], v71 offset0:2 offset1:3
	ds_read2_b64 v[72:75], v71 offset0:154 offset1:155
	s_waitcnt vmcnt(63) lgkmcnt(4)
	v_pk_fma_f32 v[76:77], v[40:41], v[80:81], v[76:77]
	v_pk_fma_f32 v[78:79], v[44:45], v[80:81], v[78:79]
	v_pk_fma_f32 v[120:121], v[48:49], v[80:81], v[120:121]
	v_pk_fma_f32 v[122:123], v[52:53], v[80:81], v[122:123]
	v_pk_fma_f32 v[76:77], v[42:43], v[82:83], v[76:77]
	v_pk_fma_f32 v[78:79], v[46:47], v[82:83], v[78:79]
	v_pk_fma_f32 v[120:121], v[50:51], v[82:83], v[120:121]
	v_pk_fma_f32 v[122:123], v[54:55], v[82:83], v[122:123]
	ds_read2_b64 v[40:43], v39 offset0:4 offset1:5
	ds_read2_b64 v[44:47], v39 offset0:156 offset1:157
	ds_read2_b64 v[48:51], v71 offset0:4 offset1:5
	ds_read2_b64 v[52:55], v71 offset0:156 offset1:157
	s_waitcnt vmcnt(63) lgkmcnt(4)
	v_pk_fma_f32 v[76:77], v[56:57], v[84:85], v[76:77]
	v_pk_fma_f32 v[78:79], v[60:61], v[84:85], v[78:79]
	v_pk_fma_f32 v[120:121], v[64:65], v[84:85], v[120:121]
	v_pk_fma_f32 v[122:123], v[72:73], v[84:85], v[122:123]
	v_pk_fma_f32 v[76:77], v[58:59], v[86:87], v[76:77]
	v_pk_fma_f32 v[78:79], v[62:63], v[86:87], v[78:79]
	v_pk_fma_f32 v[120:121], v[66:67], v[86:87], v[120:121]
	v_pk_fma_f32 v[122:123], v[74:75], v[86:87], v[122:123]
	ds_read2_b64 v[56:59], v39 offset0:6 offset1:7
	ds_read2_b64 v[60:63], v39 offset0:158 offset1:159
	ds_read2_b64 v[64:67], v71 offset0:6 offset1:7
	ds_read2_b64 v[72:75], v71 offset0:158 offset1:159
	s_waitcnt vmcnt(63) lgkmcnt(4)
	v_pk_fma_f32 v[76:77], v[40:41], v[88:89], v[76:77]
	v_pk_fma_f32 v[78:79], v[44:45], v[88:89], v[78:79]
	v_pk_fma_f32 v[120:121], v[48:49], v[88:89], v[120:121]
	v_pk_fma_f32 v[122:123], v[52:53], v[88:89], v[122:123]
	v_pk_fma_f32 v[76:77], v[42:43], v[90:91], v[76:77]
	v_pk_fma_f32 v[78:79], v[46:47], v[90:91], v[78:79]
	v_pk_fma_f32 v[120:121], v[50:51], v[90:91], v[120:121]
	v_pk_fma_f32 v[122:123], v[54:55], v[90:91], v[122:123]
	ds_read2_b64 v[40:43], v39 offset0:8 offset1:9
	ds_read2_b64 v[44:47], v39 offset0:160 offset1:161
	ds_read2_b64 v[48:51], v71 offset0:8 offset1:9
	ds_read2_b64 v[52:55], v71 offset0:160 offset1:161
	s_waitcnt vmcnt(60) lgkmcnt(4)
	v_pk_fma_f32 v[76:77], v[56:57], v[92:93], v[76:77]
	v_pk_fma_f32 v[78:79], v[60:61], v[92:93], v[78:79]
	v_pk_fma_f32 v[120:121], v[64:65], v[92:93], v[120:121]
	v_pk_fma_f32 v[122:123], v[72:73], v[92:93], v[122:123]
	v_pk_fma_f32 v[76:77], v[58:59], v[94:95], v[76:77]
	v_pk_fma_f32 v[78:79], v[62:63], v[94:95], v[78:79]
	v_pk_fma_f32 v[120:121], v[66:67], v[94:95], v[120:121]
	v_pk_fma_f32 v[122:123], v[74:75], v[94:95], v[122:123]
	ds_read2_b64 v[56:59], v39 offset0:10 offset1:11
	ds_read2_b64 v[60:63], v39 offset0:162 offset1:163
	ds_read2_b64 v[64:67], v71 offset0:10 offset1:11
	ds_read2_b64 v[72:75], v71 offset0:162 offset1:163
	s_waitcnt vmcnt(56) lgkmcnt(4)
	v_pk_fma_f32 v[76:77], v[40:41], v[96:97], v[76:77]
	v_pk_fma_f32 v[78:79], v[44:45], v[96:97], v[78:79]
	v_pk_fma_f32 v[120:121], v[48:49], v[96:97], v[120:121]
	v_pk_fma_f32 v[122:123], v[52:53], v[96:97], v[122:123]
	v_pk_fma_f32 v[76:77], v[42:43], v[98:99], v[76:77]
	v_pk_fma_f32 v[78:79], v[46:47], v[98:99], v[78:79]
	v_pk_fma_f32 v[120:121], v[50:51], v[98:99], v[120:121]
	v_pk_fma_f32 v[122:123], v[54:55], v[98:99], v[122:123]
	ds_read2_b64 v[40:43], v39 offset0:12 offset1:13
	ds_read2_b64 v[44:47], v39 offset0:164 offset1:165
	ds_read2_b64 v[48:51], v71 offset0:12 offset1:13
	ds_read2_b64 v[52:55], v71 offset0:164 offset1:165
	s_waitcnt vmcnt(52) lgkmcnt(4)
	v_pk_fma_f32 v[76:77], v[56:57], v[100:101], v[76:77]
	v_pk_fma_f32 v[78:79], v[60:61], v[100:101], v[78:79]
	v_pk_fma_f32 v[120:121], v[64:65], v[100:101], v[120:121]
	v_pk_fma_f32 v[122:123], v[72:73], v[100:101], v[122:123]
	v_pk_fma_f32 v[76:77], v[58:59], v[102:103], v[76:77]
	v_pk_fma_f32 v[78:79], v[62:63], v[102:103], v[78:79]
	v_pk_fma_f32 v[120:121], v[66:67], v[102:103], v[120:121]
	v_pk_fma_f32 v[122:123], v[74:75], v[102:103], v[122:123]
	ds_read2_b64 v[56:59], v39 offset0:14 offset1:15
	ds_read2_b64 v[60:63], v39 offset0:166 offset1:167
	ds_read2_b64 v[64:67], v71 offset0:14 offset1:15
	ds_read2_b64 v[72:75], v71 offset0:166 offset1:167
	s_waitcnt vmcnt(48) lgkmcnt(4)
	v_pk_fma_f32 v[76:77], v[40:41], v[104:105], v[76:77]
	v_pk_fma_f32 v[78:79], v[44:45], v[104:105], v[78:79]
	v_pk_fma_f32 v[120:121], v[48:49], v[104:105], v[120:121]
	v_pk_fma_f32 v[122:123], v[52:53], v[104:105], v[122:123]
	v_pk_fma_f32 v[76:77], v[42:43], v[106:107], v[76:77]
	v_pk_fma_f32 v[78:79], v[46:47], v[106:107], v[78:79]
	v_pk_fma_f32 v[120:121], v[50:51], v[106:107], v[120:121]
	v_pk_fma_f32 v[122:123], v[54:55], v[106:107], v[122:123]
	ds_read2_b64 v[40:43], v39 offset0:16 offset1:17
	ds_read2_b64 v[44:47], v39 offset0:168 offset1:169
	ds_read2_b64 v[48:51], v71 offset0:16 offset1:17
	ds_read2_b64 v[52:55], v71 offset0:168 offset1:169
	s_waitcnt vmcnt(44) lgkmcnt(4)
	v_pk_fma_f32 v[76:77], v[56:57], v[108:109], v[76:77]
	v_pk_fma_f32 v[78:79], v[60:61], v[108:109], v[78:79]
	v_pk_fma_f32 v[120:121], v[64:65], v[108:109], v[120:121]
	v_pk_fma_f32 v[122:123], v[72:73], v[108:109], v[122:123]
	v_pk_fma_f32 v[76:77], v[58:59], v[110:111], v[76:77]
	v_pk_fma_f32 v[78:79], v[62:63], v[110:111], v[78:79]
	v_pk_fma_f32 v[120:121], v[66:67], v[110:111], v[120:121]
	v_pk_fma_f32 v[122:123], v[74:75], v[110:111], v[122:123]
	ds_read2_b64 v[56:59], v39 offset0:18 offset1:19
	ds_read2_b64 v[60:63], v39 offset0:170 offset1:171
	ds_read2_b64 v[64:67], v71 offset0:18 offset1:19
	ds_read2_b64 v[72:75], v71 offset0:170 offset1:171
	s_waitcnt vmcnt(40) lgkmcnt(4)
	v_pk_fma_f32 v[76:77], v[40:41], v[112:113], v[76:77]
	v_pk_fma_f32 v[78:79], v[44:45], v[112:113], v[78:79]
	v_pk_fma_f32 v[120:121], v[48:49], v[112:113], v[120:121]
	v_pk_fma_f32 v[122:123], v[52:53], v[112:113], v[122:123]
	v_pk_fma_f32 v[76:77], v[42:43], v[114:115], v[76:77]
	v_pk_fma_f32 v[78:79], v[46:47], v[114:115], v[78:79]
	v_pk_fma_f32 v[120:121], v[50:51], v[114:115], v[120:121]
	v_pk_fma_f32 v[122:123], v[54:55], v[114:115], v[122:123]
	s_waitcnt vmcnt(38) lgkmcnt(0)
	v_pk_fma_f32 v[76:77], v[56:57], v[116:117], v[76:77]
	v_pk_fma_f32 v[78:79], v[60:61], v[116:117], v[78:79]
	v_pk_fma_f32 v[120:121], v[64:65], v[116:117], v[120:121]
	v_pk_fma_f32 v[122:123], v[72:73], v[116:117], v[122:123]
	v_mul_u32_u24_e32 v92, 0x4c, v1
	v_add_u32_e32 v92, 0xfb00, v92
	v_add_u32_e32 v93, 0x4c0, v92
	v_add_u32_e32 v94, 0x980, v92
	v_add_u32_e32 v95, 0xe40, v92
	v_add_u32_e32 v96, 0x1300, v92
	v_mov_b32_e32 v97, 0x427c0000
	s_mov_b32 s0, 0xc27c0000
	v_mov_b32_e32 v124, 1.0
	v_mov_b32_e32 v125, 1.0
	v_mov_b32_e32 v126, 0x4038aa3b
	v_mov_b32_e32 v127, 0x4038aa3b
	v_mov_b32_e32 v80, 0
	v_mov_b32_e32 v81, 0
	v_mov_b32_e32 v82, 0
	v_mov_b32_e32 v83, 0
	v_mov_b32_e32 v84, 0
	v_mov_b32_e32 v85, 0
	v_mov_b32_e32 v86, 0
	v_mov_b32_e32 v87, 0
	v_mov_b32_e32 v88, 0
	v_mov_b32_e32 v89, 0
	ds_read2_b32 v[40:41], v92 offset0:0 offset1:152
	ds_read2_b32 v[42:43], v93 offset0:0 offset1:152
	ds_read2_b32 v[44:45], v94 offset0:0 offset1:152
	ds_read2_b32 v[46:47], v95 offset0:0 offset1:152
	ds_read2_b32 v[48:49], v96 offset0:0 offset1:152
	s_waitcnt vmcnt(36)
	v_pk_mul_f32 v[90:91], v[2:3], v[126:127]
	s_nop 0
	v_med3_f32 v90, v90, s0, v97
	v_med3_f32 v91, v91, s0, v97
	v_exp_f32_e32 v68, v90
	v_exp_f32_e32 v69, v91
	s_waitcnt lgkmcnt(0)
	ds_read2_b32 v[50:51], v92 offset0:1 offset1:153
	ds_read2_b32 v[52:53], v93 offset0:1 offset1:153
	ds_read2_b32 v[54:55], v94 offset0:1 offset1:153
	ds_read2_b32 v[56:57], v95 offset0:1 offset1:153
	ds_read2_b32 v[58:59], v96 offset0:1 offset1:153
	v_pk_add_f32 v[88:89], v[88:89], v[48:49]
	v_pk_add_f32 v[74:75], v[48:49], v[48:49]
	v_pk_fma_f32 v[60:61], v[68:69], v[40:41], v[124:125] op_sel_hi:[0,1,1]
	v_pk_fma_f32 v[62:63], v[68:69], v[42:43], v[124:125] op_sel_hi:[0,1,1]
	v_pk_fma_f32 v[64:65], v[68:69], v[44:45], v[124:125] op_sel:[1,0,0]
	v_pk_fma_f32 v[66:67], v[68:69], v[46:47], v[124:125] op_sel:[1,0,0]
	v_rcp_f32_e32 v60, v60
	v_rcp_f32_e32 v61, v61
	v_rcp_f32_e32 v62, v62
	v_rcp_f32_e32 v63, v63
	v_rcp_f32_e32 v64, v64
	v_rcp_f32_e32 v65, v65
	v_rcp_f32_e32 v66, v66
	v_rcp_f32_e32 v67, v67
	s_waitcnt vmcnt(34)
	v_pk_mul_f32 v[90:91], v[4:5], v[126:127]
	s_nop 0
	v_med3_f32 v90, v90, s0, v97
	v_med3_f32 v91, v91, s0, v97
	v_exp_f32_e32 v72, v90
	v_exp_f32_e32 v73, v91
	v_pk_fma_f32 v[80:81], v[74:75], v[60:61], v[80:81] op_sel_hi:[0,1,1] neg_lo:[1,0,0] neg_hi:[1,0,0]
	v_pk_fma_f32 v[82:83], v[74:75], v[62:63], v[82:83] op_sel_hi:[0,1,1] neg_lo:[1,0,0] neg_hi:[1,0,0]
	v_pk_fma_f32 v[84:85], v[74:75], v[64:65], v[84:85] op_sel:[1,0,0] neg_lo:[1,0,0] neg_hi:[1,0,0]
	v_pk_fma_f32 v[86:87], v[74:75], v[66:67], v[86:87] op_sel:[1,0,0] neg_lo:[1,0,0] neg_hi:[1,0,0]
	s_waitcnt lgkmcnt(0)
	ds_read2_b32 v[40:41], v92 offset0:2 offset1:154
	ds_read2_b32 v[42:43], v93 offset0:2 offset1:154
	ds_read2_b32 v[44:45], v94 offset0:2 offset1:154
	ds_read2_b32 v[46:47], v95 offset0:2 offset1:154
	ds_read2_b32 v[48:49], v96 offset0:2 offset1:154
	v_pk_add_f32 v[88:89], v[88:89], v[58:59]
	v_pk_add_f32 v[74:75], v[58:59], v[58:59]
	v_pk_fma_f32 v[60:61], v[72:73], v[50:51], v[124:125] op_sel_hi:[0,1,1]
	v_pk_fma_f32 v[62:63], v[72:73], v[52:53], v[124:125] op_sel_hi:[0,1,1]
	v_pk_fma_f32 v[64:65], v[72:73], v[54:55], v[124:125] op_sel:[1,0,0]
	v_pk_fma_f32 v[66:67], v[72:73], v[56:57], v[124:125] op_sel:[1,0,0]
	v_rcp_f32_e32 v60, v60
	v_rcp_f32_e32 v61, v61
	v_rcp_f32_e32 v62, v62
	v_rcp_f32_e32 v63, v63
	v_rcp_f32_e32 v64, v64
	v_rcp_f32_e32 v65, v65
	v_rcp_f32_e32 v66, v66
	v_rcp_f32_e32 v67, v67
	s_waitcnt vmcnt(32)
	v_pk_mul_f32 v[90:91], v[6:7], v[126:127]
	s_nop 0
	v_med3_f32 v90, v90, s0, v97
	v_med3_f32 v91, v91, s0, v97
	v_exp_f32_e32 v68, v90
	v_exp_f32_e32 v69, v91
	v_pk_fma_f32 v[80:81], v[74:75], v[60:61], v[80:81] op_sel_hi:[0,1,1] neg_lo:[1,0,0] neg_hi:[1,0,0]
	v_pk_fma_f32 v[82:83], v[74:75], v[62:63], v[82:83] op_sel_hi:[0,1,1] neg_lo:[1,0,0] neg_hi:[1,0,0]
	v_pk_fma_f32 v[84:85], v[74:75], v[64:65], v[84:85] op_sel:[1,0,0] neg_lo:[1,0,0] neg_hi:[1,0,0]
	v_pk_fma_f32 v[86:87], v[74:75], v[66:67], v[86:87] op_sel:[1,0,0] neg_lo:[1,0,0] neg_hi:[1,0,0]
	s_waitcnt lgkmcnt(0)
	ds_read2_b32 v[50:51], v92 offset0:3 offset1:155
	ds_read2_b32 v[52:53], v93 offset0:3 offset1:155
	ds_read2_b32 v[54:55], v94 offset0:3 offset1:155
	ds_read2_b32 v[56:57], v95 offset0:3 offset1:155
	ds_read2_b32 v[58:59], v96 offset0:3 offset1:155
	v_pk_add_f32 v[88:89], v[88:89], v[48:49]
	v_pk_add_f32 v[74:75], v[48:49], v[48:49]
	v_pk_fma_f32 v[60:61], v[68:69], v[40:41], v[124:125] op_sel_hi:[0,1,1]
	v_pk_fma_f32 v[62:63], v[68:69], v[42:43], v[124:125] op_sel_hi:[0,1,1]
	v_pk_fma_f32 v[64:65], v[68:69], v[44:45], v[124:125] op_sel:[1,0,0]
	v_pk_fma_f32 v[66:67], v[68:69], v[46:47], v[124:125] op_sel:[1,0,0]
	v_rcp_f32_e32 v60, v60
	v_rcp_f32_e32 v61, v61
	v_rcp_f32_e32 v62, v62
	v_rcp_f32_e32 v63, v63
	v_rcp_f32_e32 v64, v64
	v_rcp_f32_e32 v65, v65
	v_rcp_f32_e32 v66, v66
	v_rcp_f32_e32 v67, v67
	s_waitcnt vmcnt(30)
	v_pk_mul_f32 v[90:91], v[8:9], v[126:127]
	s_nop 0
	v_med3_f32 v90, v90, s0, v97
	v_med3_f32 v91, v91, s0, v97
	v_exp_f32_e32 v72, v90
	v_exp_f32_e32 v73, v91
	v_pk_fma_f32 v[80:81], v[74:75], v[60:61], v[80:81] op_sel_hi:[0,1,1] neg_lo:[1,0,0] neg_hi:[1,0,0]
	v_pk_fma_f32 v[82:83], v[74:75], v[62:63], v[82:83] op_sel_hi:[0,1,1] neg_lo:[1,0,0] neg_hi:[1,0,0]
	v_pk_fma_f32 v[84:85], v[74:75], v[64:65], v[84:85] op_sel:[1,0,0] neg_lo:[1,0,0] neg_hi:[1,0,0]
	v_pk_fma_f32 v[86:87], v[74:75], v[66:67], v[86:87] op_sel:[1,0,0] neg_lo:[1,0,0] neg_hi:[1,0,0]
	s_waitcnt lgkmcnt(0)
	ds_read2_b32 v[40:41], v92 offset0:4 offset1:156
	ds_read2_b32 v[42:43], v93 offset0:4 offset1:156
	ds_read2_b32 v[44:45], v94 offset0:4 offset1:156
	ds_read2_b32 v[46:47], v95 offset0:4 offset1:156
	ds_read2_b32 v[48:49], v96 offset0:4 offset1:156
	v_pk_add_f32 v[88:89], v[88:89], v[58:59]
	v_pk_add_f32 v[74:75], v[58:59], v[58:59]
	v_pk_fma_f32 v[60:61], v[72:73], v[50:51], v[124:125] op_sel_hi:[0,1,1]
	v_pk_fma_f32 v[62:63], v[72:73], v[52:53], v[124:125] op_sel_hi:[0,1,1]
	v_pk_fma_f32 v[64:65], v[72:73], v[54:55], v[124:125] op_sel:[1,0,0]
	v_pk_fma_f32 v[66:67], v[72:73], v[56:57], v[124:125] op_sel:[1,0,0]
	v_rcp_f32_e32 v60, v60
	v_rcp_f32_e32 v61, v61
	v_rcp_f32_e32 v62, v62
	v_rcp_f32_e32 v63, v63
	v_rcp_f32_e32 v64, v64
	v_rcp_f32_e32 v65, v65
	v_rcp_f32_e32 v66, v66
	v_rcp_f32_e32 v67, v67
	s_waitcnt vmcnt(28)
	v_pk_mul_f32 v[90:91], v[10:11], v[126:127]
	s_nop 0
	v_med3_f32 v90, v90, s0, v97
	v_med3_f32 v91, v91, s0, v97
	v_exp_f32_e32 v68, v90
	v_exp_f32_e32 v69, v91
	v_pk_fma_f32 v[80:81], v[74:75], v[60:61], v[80:81] op_sel_hi:[0,1,1] neg_lo:[1,0,0] neg_hi:[1,0,0]
	v_pk_fma_f32 v[82:83], v[74:75], v[62:63], v[82:83] op_sel_hi:[0,1,1] neg_lo:[1,0,0] neg_hi:[1,0,0]
	v_pk_fma_f32 v[84:85], v[74:75], v[64:65], v[84:85] op_sel:[1,0,0] neg_lo:[1,0,0] neg_hi:[1,0,0]
	v_pk_fma_f32 v[86:87], v[74:75], v[66:67], v[86:87] op_sel:[1,0,0] neg_lo:[1,0,0] neg_hi:[1,0,0]
	s_waitcnt lgkmcnt(0)
	ds_read2_b32 v[50:51], v92 offset0:5 offset1:157
	ds_read2_b32 v[52:53], v93 offset0:5 offset1:157
	ds_read2_b32 v[54:55], v94 offset0:5 offset1:157
	ds_read2_b32 v[56:57], v95 offset0:5 offset1:157
	ds_read2_b32 v[58:59], v96 offset0:5 offset1:157
	v_pk_add_f32 v[88:89], v[88:89], v[48:49]
	v_pk_add_f32 v[74:75], v[48:49], v[48:49]
	v_pk_fma_f32 v[60:61], v[68:69], v[40:41], v[124:125] op_sel_hi:[0,1,1]
	v_pk_fma_f32 v[62:63], v[68:69], v[42:43], v[124:125] op_sel_hi:[0,1,1]
	v_pk_fma_f32 v[64:65], v[68:69], v[44:45], v[124:125] op_sel:[1,0,0]
	v_pk_fma_f32 v[66:67], v[68:69], v[46:47], v[124:125] op_sel:[1,0,0]
	v_rcp_f32_e32 v60, v60
	v_rcp_f32_e32 v61, v61
	v_rcp_f32_e32 v62, v62
	v_rcp_f32_e32 v63, v63
	v_rcp_f32_e32 v64, v64
	v_rcp_f32_e32 v65, v65
	v_rcp_f32_e32 v66, v66
	v_rcp_f32_e32 v67, v67
	s_waitcnt vmcnt(26)
	v_pk_mul_f32 v[90:91], v[12:13], v[126:127]
	s_nop 0
	v_med3_f32 v90, v90, s0, v97
	v_med3_f32 v91, v91, s0, v97
	v_exp_f32_e32 v72, v90
	v_exp_f32_e32 v73, v91
	v_pk_fma_f32 v[80:81], v[74:75], v[60:61], v[80:81] op_sel_hi:[0,1,1] neg_lo:[1,0,0] neg_hi:[1,0,0]
	v_pk_fma_f32 v[82:83], v[74:75], v[62:63], v[82:83] op_sel_hi:[0,1,1] neg_lo:[1,0,0] neg_hi:[1,0,0]
	v_pk_fma_f32 v[84:85], v[74:75], v[64:65], v[84:85] op_sel:[1,0,0] neg_lo:[1,0,0] neg_hi:[1,0,0]
	v_pk_fma_f32 v[86:87], v[74:75], v[66:67], v[86:87] op_sel:[1,0,0] neg_lo:[1,0,0] neg_hi:[1,0,0]
	s_waitcnt lgkmcnt(0)
	ds_read2_b32 v[40:41], v92 offset0:6 offset1:158
	ds_read2_b32 v[42:43], v93 offset0:6 offset1:158
	ds_read2_b32 v[44:45], v94 offset0:6 offset1:158
	ds_read2_b32 v[46:47], v95 offset0:6 offset1:158
	ds_read2_b32 v[48:49], v96 offset0:6 offset1:158
	v_pk_add_f32 v[88:89], v[88:89], v[58:59]
	v_pk_add_f32 v[74:75], v[58:59], v[58:59]
	v_pk_fma_f32 v[60:61], v[72:73], v[50:51], v[124:125] op_sel_hi:[0,1,1]
	v_pk_fma_f32 v[62:63], v[72:73], v[52:53], v[124:125] op_sel_hi:[0,1,1]
	v_pk_fma_f32 v[64:65], v[72:73], v[54:55], v[124:125] op_sel:[1,0,0]
	v_pk_fma_f32 v[66:67], v[72:73], v[56:57], v[124:125] op_sel:[1,0,0]
	v_rcp_f32_e32 v60, v60
	v_rcp_f32_e32 v61, v61
	v_rcp_f32_e32 v62, v62
	v_rcp_f32_e32 v63, v63
	v_rcp_f32_e32 v64, v64
	v_rcp_f32_e32 v65, v65
	v_rcp_f32_e32 v66, v66
	v_rcp_f32_e32 v67, v67
	s_waitcnt vmcnt(24)
	v_pk_mul_f32 v[90:91], v[14:15], v[126:127]
	s_nop 0
	v_med3_f32 v90, v90, s0, v97
	v_med3_f32 v91, v91, s0, v97
	v_exp_f32_e32 v68, v90
	v_exp_f32_e32 v69, v91
	v_pk_fma_f32 v[80:81], v[74:75], v[60:61], v[80:81] op_sel_hi:[0,1,1] neg_lo:[1,0,0] neg_hi:[1,0,0]
	v_pk_fma_f32 v[82:83], v[74:75], v[62:63], v[82:83] op_sel_hi:[0,1,1] neg_lo:[1,0,0] neg_hi:[1,0,0]
	v_pk_fma_f32 v[84:85], v[74:75], v[64:65], v[84:85] op_sel:[1,0,0] neg_lo:[1,0,0] neg_hi:[1,0,0]
	v_pk_fma_f32 v[86:87], v[74:75], v[66:67], v[86:87] op_sel:[1,0,0] neg_lo:[1,0,0] neg_hi:[1,0,0]
	s_waitcnt lgkmcnt(0)
	ds_read2_b32 v[50:51], v92 offset0:7 offset1:159
	ds_read2_b32 v[52:53], v93 offset0:7 offset1:159
	ds_read2_b32 v[54:55], v94 offset0:7 offset1:159
	ds_read2_b32 v[56:57], v95 offset0:7 offset1:159
	ds_read2_b32 v[58:59], v96 offset0:7 offset1:159
	v_pk_add_f32 v[88:89], v[88:89], v[48:49]
	v_pk_add_f32 v[74:75], v[48:49], v[48:49]
	v_pk_fma_f32 v[60:61], v[68:69], v[40:41], v[124:125] op_sel_hi:[0,1,1]
	v_pk_fma_f32 v[62:63], v[68:69], v[42:43], v[124:125] op_sel_hi:[0,1,1]
	v_pk_fma_f32 v[64:65], v[68:69], v[44:45], v[124:125] op_sel:[1,0,0]
	v_pk_fma_f32 v[66:67], v[68:69], v[46:47], v[124:125] op_sel:[1,0,0]
	v_rcp_f32_e32 v60, v60
	v_rcp_f32_e32 v61, v61
	v_rcp_f32_e32 v62, v62
	v_rcp_f32_e32 v63, v63
	v_rcp_f32_e32 v64, v64
	v_rcp_f32_e32 v65, v65
	v_rcp_f32_e32 v66, v66
	v_rcp_f32_e32 v67, v67
	s_waitcnt vmcnt(22)
	v_pk_mul_f32 v[90:91], v[16:17], v[126:127]
	s_nop 0
	v_med3_f32 v90, v90, s0, v97
	v_med3_f32 v91, v91, s0, v97
	v_exp_f32_e32 v72, v90
	v_exp_f32_e32 v73, v91
	v_pk_fma_f32 v[80:81], v[74:75], v[60:61], v[80:81] op_sel_hi:[0,1,1] neg_lo:[1,0,0] neg_hi:[1,0,0]
	v_pk_fma_f32 v[82:83], v[74:75], v[62:63], v[82:83] op_sel_hi:[0,1,1] neg_lo:[1,0,0] neg_hi:[1,0,0]
	v_pk_fma_f32 v[84:85], v[74:75], v[64:65], v[84:85] op_sel:[1,0,0] neg_lo:[1,0,0] neg_hi:[1,0,0]
	v_pk_fma_f32 v[86:87], v[74:75], v[66:67], v[86:87] op_sel:[1,0,0] neg_lo:[1,0,0] neg_hi:[1,0,0]
	s_waitcnt lgkmcnt(0)
	ds_read2_b32 v[40:41], v92 offset0:8 offset1:160
	ds_read2_b32 v[42:43], v93 offset0:8 offset1:160
	ds_read2_b32 v[44:45], v94 offset0:8 offset1:160
	ds_read2_b32 v[46:47], v95 offset0:8 offset1:160
	ds_read2_b32 v[48:49], v96 offset0:8 offset1:160
	v_pk_add_f32 v[88:89], v[88:89], v[58:59]
	v_pk_add_f32 v[74:75], v[58:59], v[58:59]
	v_pk_fma_f32 v[60:61], v[72:73], v[50:51], v[124:125] op_sel_hi:[0,1,1]
	v_pk_fma_f32 v[62:63], v[72:73], v[52:53], v[124:125] op_sel_hi:[0,1,1]
	v_pk_fma_f32 v[64:65], v[72:73], v[54:55], v[124:125] op_sel:[1,0,0]
	v_pk_fma_f32 v[66:67], v[72:73], v[56:57], v[124:125] op_sel:[1,0,0]
	v_rcp_f32_e32 v60, v60
	v_rcp_f32_e32 v61, v61
	v_rcp_f32_e32 v62, v62
	v_rcp_f32_e32 v63, v63
	v_rcp_f32_e32 v64, v64
	v_rcp_f32_e32 v65, v65
	v_rcp_f32_e32 v66, v66
	v_rcp_f32_e32 v67, v67
	s_waitcnt vmcnt(20)
	v_pk_mul_f32 v[90:91], v[18:19], v[126:127]
	s_nop 0
	v_med3_f32 v90, v90, s0, v97
	v_med3_f32 v91, v91, s0, v97
	v_exp_f32_e32 v68, v90
	v_exp_f32_e32 v69, v91
	v_pk_fma_f32 v[80:81], v[74:75], v[60:61], v[80:81] op_sel_hi:[0,1,1] neg_lo:[1,0,0] neg_hi:[1,0,0]
	v_pk_fma_f32 v[82:83], v[74:75], v[62:63], v[82:83] op_sel_hi:[0,1,1] neg_lo:[1,0,0] neg_hi:[1,0,0]
	v_pk_fma_f32 v[84:85], v[74:75], v[64:65], v[84:85] op_sel:[1,0,0] neg_lo:[1,0,0] neg_hi:[1,0,0]
	v_pk_fma_f32 v[86:87], v[74:75], v[66:67], v[86:87] op_sel:[1,0,0] neg_lo:[1,0,0] neg_hi:[1,0,0]
	s_waitcnt lgkmcnt(0)
	ds_read2_b32 v[50:51], v92 offset0:9 offset1:161
	ds_read2_b32 v[52:53], v93 offset0:9 offset1:161
	ds_read2_b32 v[54:55], v94 offset0:9 offset1:161
	ds_read2_b32 v[56:57], v95 offset0:9 offset1:161
	ds_read2_b32 v[58:59], v96 offset0:9 offset1:161
	v_pk_add_f32 v[88:89], v[88:89], v[48:49]
	v_pk_add_f32 v[74:75], v[48:49], v[48:49]
	v_pk_fma_f32 v[60:61], v[68:69], v[40:41], v[124:125] op_sel_hi:[0,1,1]
	v_pk_fma_f32 v[62:63], v[68:69], v[42:43], v[124:125] op_sel_hi:[0,1,1]
	v_pk_fma_f32 v[64:65], v[68:69], v[44:45], v[124:125] op_sel:[1,0,0]
	v_pk_fma_f32 v[66:67], v[68:69], v[46:47], v[124:125] op_sel:[1,0,0]
	v_rcp_f32_e32 v60, v60
	v_rcp_f32_e32 v61, v61
	v_rcp_f32_e32 v62, v62
	v_rcp_f32_e32 v63, v63
	v_rcp_f32_e32 v64, v64
	v_rcp_f32_e32 v65, v65
	v_rcp_f32_e32 v66, v66
	v_rcp_f32_e32 v67, v67
	s_waitcnt vmcnt(18)
	v_pk_mul_f32 v[90:91], v[20:21], v[126:127]
	s_nop 0
	v_med3_f32 v90, v90, s0, v97
	v_med3_f32 v91, v91, s0, v97
	v_exp_f32_e32 v72, v90
	v_exp_f32_e32 v73, v91
	v_pk_fma_f32 v[80:81], v[74:75], v[60:61], v[80:81] op_sel_hi:[0,1,1] neg_lo:[1,0,0] neg_hi:[1,0,0]
	v_pk_fma_f32 v[82:83], v[74:75], v[62:63], v[82:83] op_sel_hi:[0,1,1] neg_lo:[1,0,0] neg_hi:[1,0,0]
	v_pk_fma_f32 v[84:85], v[74:75], v[64:65], v[84:85] op_sel:[1,0,0] neg_lo:[1,0,0] neg_hi:[1,0,0]
	v_pk_fma_f32 v[86:87], v[74:75], v[66:67], v[86:87] op_sel:[1,0,0] neg_lo:[1,0,0] neg_hi:[1,0,0]
	s_waitcnt lgkmcnt(0)
	ds_read2_b32 v[40:41], v92 offset0:10 offset1:162
	ds_read2_b32 v[42:43], v93 offset0:10 offset1:162
	ds_read2_b32 v[44:45], v94 offset0:10 offset1:162
	ds_read2_b32 v[46:47], v95 offset0:10 offset1:162
	ds_read2_b32 v[48:49], v96 offset0:10 offset1:162
	v_pk_add_f32 v[88:89], v[88:89], v[58:59]
	v_pk_add_f32 v[74:75], v[58:59], v[58:59]
	v_pk_fma_f32 v[60:61], v[72:73], v[50:51], v[124:125] op_sel_hi:[0,1,1]
	v_pk_fma_f32 v[62:63], v[72:73], v[52:53], v[124:125] op_sel_hi:[0,1,1]
	v_pk_fma_f32 v[64:65], v[72:73], v[54:55], v[124:125] op_sel:[1,0,0]
	v_pk_fma_f32 v[66:67], v[72:73], v[56:57], v[124:125] op_sel:[1,0,0]
	v_rcp_f32_e32 v60, v60
	v_rcp_f32_e32 v61, v61
	v_rcp_f32_e32 v62, v62
	v_rcp_f32_e32 v63, v63
	v_rcp_f32_e32 v64, v64
	v_rcp_f32_e32 v65, v65
	v_rcp_f32_e32 v66, v66
	v_rcp_f32_e32 v67, v67
	s_waitcnt vmcnt(16)
	v_pk_mul_f32 v[90:91], v[22:23], v[126:127]
	s_nop 0
	v_med3_f32 v90, v90, s0, v97
	v_med3_f32 v91, v91, s0, v97
	v_exp_f32_e32 v68, v90
	v_exp_f32_e32 v69, v91
	v_pk_fma_f32 v[80:81], v[74:75], v[60:61], v[80:81] op_sel_hi:[0,1,1] neg_lo:[1,0,0] neg_hi:[1,0,0]
	v_pk_fma_f32 v[82:83], v[74:75], v[62:63], v[82:83] op_sel_hi:[0,1,1] neg_lo:[1,0,0] neg_hi:[1,0,0]
	v_pk_fma_f32 v[84:85], v[74:75], v[64:65], v[84:85] op_sel:[1,0,0] neg_lo:[1,0,0] neg_hi:[1,0,0]
	v_pk_fma_f32 v[86:87], v[74:75], v[66:67], v[86:87] op_sel:[1,0,0] neg_lo:[1,0,0] neg_hi:[1,0,0]
	s_waitcnt lgkmcnt(0)
	ds_read2_b32 v[50:51], v92 offset0:11 offset1:163
	ds_read2_b32 v[52:53], v93 offset0:11 offset1:163
	ds_read2_b32 v[54:55], v94 offset0:11 offset1:163
	ds_read2_b32 v[56:57], v95 offset0:11 offset1:163
	ds_read2_b32 v[58:59], v96 offset0:11 offset1:163
	v_pk_add_f32 v[88:89], v[88:89], v[48:49]
	v_pk_add_f32 v[74:75], v[48:49], v[48:49]
	v_pk_fma_f32 v[60:61], v[68:69], v[40:41], v[124:125] op_sel_hi:[0,1,1]
	v_pk_fma_f32 v[62:63], v[68:69], v[42:43], v[124:125] op_sel_hi:[0,1,1]
	v_pk_fma_f32 v[64:65], v[68:69], v[44:45], v[124:125] op_sel:[1,0,0]
	v_pk_fma_f32 v[66:67], v[68:69], v[46:47], v[124:125] op_sel:[1,0,0]
	v_rcp_f32_e32 v60, v60
	v_rcp_f32_e32 v61, v61
	v_rcp_f32_e32 v62, v62
	v_rcp_f32_e32 v63, v63
	v_rcp_f32_e32 v64, v64
	v_rcp_f32_e32 v65, v65
	v_rcp_f32_e32 v66, v66
	v_rcp_f32_e32 v67, v67
	s_waitcnt vmcnt(14)
	v_pk_mul_f32 v[90:91], v[24:25], v[126:127]
	s_nop 0
	v_med3_f32 v90, v90, s0, v97
	v_med3_f32 v91, v91, s0, v97
	v_exp_f32_e32 v72, v90
	v_exp_f32_e32 v73, v91
	v_pk_fma_f32 v[80:81], v[74:75], v[60:61], v[80:81] op_sel_hi:[0,1,1] neg_lo:[1,0,0] neg_hi:[1,0,0]
	v_pk_fma_f32 v[82:83], v[74:75], v[62:63], v[82:83] op_sel_hi:[0,1,1] neg_lo:[1,0,0] neg_hi:[1,0,0]
	v_pk_fma_f32 v[84:85], v[74:75], v[64:65], v[84:85] op_sel:[1,0,0] neg_lo:[1,0,0] neg_hi:[1,0,0]
	v_pk_fma_f32 v[86:87], v[74:75], v[66:67], v[86:87] op_sel:[1,0,0] neg_lo:[1,0,0] neg_hi:[1,0,0]
	s_waitcnt lgkmcnt(0)
	ds_read2_b32 v[40:41], v92 offset0:12 offset1:164
	ds_read2_b32 v[42:43], v93 offset0:12 offset1:164
	ds_read2_b32 v[44:45], v94 offset0:12 offset1:164
	ds_read2_b32 v[46:47], v95 offset0:12 offset1:164
	ds_read2_b32 v[48:49], v96 offset0:12 offset1:164
	v_pk_add_f32 v[88:89], v[88:89], v[58:59]
	v_pk_add_f32 v[74:75], v[58:59], v[58:59]
	v_pk_fma_f32 v[60:61], v[72:73], v[50:51], v[124:125] op_sel_hi:[0,1,1]
	v_pk_fma_f32 v[62:63], v[72:73], v[52:53], v[124:125] op_sel_hi:[0,1,1]
	v_pk_fma_f32 v[64:65], v[72:73], v[54:55], v[124:125] op_sel:[1,0,0]
	v_pk_fma_f32 v[66:67], v[72:73], v[56:57], v[124:125] op_sel:[1,0,0]
	v_rcp_f32_e32 v60, v60
	v_rcp_f32_e32 v61, v61
	v_rcp_f32_e32 v62, v62
	v_rcp_f32_e32 v63, v63
	v_rcp_f32_e32 v64, v64
	v_rcp_f32_e32 v65, v65
	v_rcp_f32_e32 v66, v66
	v_rcp_f32_e32 v67, v67
	s_waitcnt vmcnt(12)
	v_pk_mul_f32 v[90:91], v[26:27], v[126:127]
	s_nop 0
	v_med3_f32 v90, v90, s0, v97
	v_med3_f32 v91, v91, s0, v97
	v_exp_f32_e32 v68, v90
	v_exp_f32_e32 v69, v91
	v_pk_fma_f32 v[80:81], v[74:75], v[60:61], v[80:81] op_sel_hi:[0,1,1] neg_lo:[1,0,0] neg_hi:[1,0,0]
	v_pk_fma_f32 v[82:83], v[74:75], v[62:63], v[82:83] op_sel_hi:[0,1,1] neg_lo:[1,0,0] neg_hi:[1,0,0]
	v_pk_fma_f32 v[84:85], v[74:75], v[64:65], v[84:85] op_sel:[1,0,0] neg_lo:[1,0,0] neg_hi:[1,0,0]
	v_pk_fma_f32 v[86:87], v[74:75], v[66:67], v[86:87] op_sel:[1,0,0] neg_lo:[1,0,0] neg_hi:[1,0,0]
	s_waitcnt lgkmcnt(0)
	ds_read2_b32 v[50:51], v92 offset0:13 offset1:165
	ds_read2_b32 v[52:53], v93 offset0:13 offset1:165
	ds_read2_b32 v[54:55], v94 offset0:13 offset1:165
	ds_read2_b32 v[56:57], v95 offset0:13 offset1:165
	ds_read2_b32 v[58:59], v96 offset0:13 offset1:165
	v_pk_add_f32 v[88:89], v[88:89], v[48:49]
	v_pk_add_f32 v[74:75], v[48:49], v[48:49]
	v_pk_fma_f32 v[60:61], v[68:69], v[40:41], v[124:125] op_sel_hi:[0,1,1]
	v_pk_fma_f32 v[62:63], v[68:69], v[42:43], v[124:125] op_sel_hi:[0,1,1]
	v_pk_fma_f32 v[64:65], v[68:69], v[44:45], v[124:125] op_sel:[1,0,0]
	v_pk_fma_f32 v[66:67], v[68:69], v[46:47], v[124:125] op_sel:[1,0,0]
	v_rcp_f32_e32 v60, v60
	v_rcp_f32_e32 v61, v61
	v_rcp_f32_e32 v62, v62
	v_rcp_f32_e32 v63, v63
	v_rcp_f32_e32 v64, v64
	v_rcp_f32_e32 v65, v65
	v_rcp_f32_e32 v66, v66
	v_rcp_f32_e32 v67, v67
	s_waitcnt vmcnt(10)
	v_pk_mul_f32 v[90:91], v[28:29], v[126:127]
	s_nop 0
	v_med3_f32 v90, v90, s0, v97
	v_med3_f32 v91, v91, s0, v97
	v_exp_f32_e32 v72, v90
	v_exp_f32_e32 v73, v91
	v_pk_fma_f32 v[80:81], v[74:75], v[60:61], v[80:81] op_sel_hi:[0,1,1] neg_lo:[1,0,0] neg_hi:[1,0,0]
	v_pk_fma_f32 v[82:83], v[74:75], v[62:63], v[82:83] op_sel_hi:[0,1,1] neg_lo:[1,0,0] neg_hi:[1,0,0]
	v_pk_fma_f32 v[84:85], v[74:75], v[64:65], v[84:85] op_sel:[1,0,0] neg_lo:[1,0,0] neg_hi:[1,0,0]
	v_pk_fma_f32 v[86:87], v[74:75], v[66:67], v[86:87] op_sel:[1,0,0] neg_lo:[1,0,0] neg_hi:[1,0,0]
	s_waitcnt lgkmcnt(0)
	ds_read2_b32 v[40:41], v92 offset0:14 offset1:166
	ds_read2_b32 v[42:43], v93 offset0:14 offset1:166
	ds_read2_b32 v[44:45], v94 offset0:14 offset1:166
	ds_read2_b32 v[46:47], v95 offset0:14 offset1:166
	ds_read2_b32 v[48:49], v96 offset0:14 offset1:166
	v_pk_add_f32 v[88:89], v[88:89], v[58:59]
	v_pk_add_f32 v[74:75], v[58:59], v[58:59]
	v_pk_fma_f32 v[60:61], v[72:73], v[50:51], v[124:125] op_sel_hi:[0,1,1]
	v_pk_fma_f32 v[62:63], v[72:73], v[52:53], v[124:125] op_sel_hi:[0,1,1]
	v_pk_fma_f32 v[64:65], v[72:73], v[54:55], v[124:125] op_sel:[1,0,0]
	v_pk_fma_f32 v[66:67], v[72:73], v[56:57], v[124:125] op_sel:[1,0,0]
	v_rcp_f32_e32 v60, v60
	v_rcp_f32_e32 v61, v61
	v_rcp_f32_e32 v62, v62
	v_rcp_f32_e32 v63, v63
	v_rcp_f32_e32 v64, v64
	v_rcp_f32_e32 v65, v65
	v_rcp_f32_e32 v66, v66
	v_rcp_f32_e32 v67, v67
	s_waitcnt vmcnt(8)
	v_pk_mul_f32 v[90:91], v[30:31], v[126:127]
	s_nop 0
	v_med3_f32 v90, v90, s0, v97
	v_med3_f32 v91, v91, s0, v97
	v_exp_f32_e32 v68, v90
	v_exp_f32_e32 v69, v91
	v_pk_fma_f32 v[80:81], v[74:75], v[60:61], v[80:81] op_sel_hi:[0,1,1] neg_lo:[1,0,0] neg_hi:[1,0,0]
	v_pk_fma_f32 v[82:83], v[74:75], v[62:63], v[82:83] op_sel_hi:[0,1,1] neg_lo:[1,0,0] neg_hi:[1,0,0]
	v_pk_fma_f32 v[84:85], v[74:75], v[64:65], v[84:85] op_sel:[1,0,0] neg_lo:[1,0,0] neg_hi:[1,0,0]
	v_pk_fma_f32 v[86:87], v[74:75], v[66:67], v[86:87] op_sel:[1,0,0] neg_lo:[1,0,0] neg_hi:[1,0,0]
	s_waitcnt lgkmcnt(0)
	ds_read2_b32 v[50:51], v92 offset0:15 offset1:167
	ds_read2_b32 v[52:53], v93 offset0:15 offset1:167
	ds_read2_b32 v[54:55], v94 offset0:15 offset1:167
	ds_read2_b32 v[56:57], v95 offset0:15 offset1:167
	ds_read2_b32 v[58:59], v96 offset0:15 offset1:167
	v_pk_add_f32 v[88:89], v[88:89], v[48:49]
	v_pk_add_f32 v[74:75], v[48:49], v[48:49]
	v_pk_fma_f32 v[60:61], v[68:69], v[40:41], v[124:125] op_sel_hi:[0,1,1]
	v_pk_fma_f32 v[62:63], v[68:69], v[42:43], v[124:125] op_sel_hi:[0,1,1]
	v_pk_fma_f32 v[64:65], v[68:69], v[44:45], v[124:125] op_sel:[1,0,0]
	v_pk_fma_f32 v[66:67], v[68:69], v[46:47], v[124:125] op_sel:[1,0,0]
	v_rcp_f32_e32 v60, v60
	v_rcp_f32_e32 v61, v61
	v_rcp_f32_e32 v62, v62
	v_rcp_f32_e32 v63, v63
	v_rcp_f32_e32 v64, v64
	v_rcp_f32_e32 v65, v65
	v_rcp_f32_e32 v66, v66
	v_rcp_f32_e32 v67, v67
	s_waitcnt vmcnt(6)
	v_pk_mul_f32 v[90:91], v[32:33], v[126:127]
	s_nop 0
	v_med3_f32 v90, v90, s0, v97
	v_med3_f32 v91, v91, s0, v97
	v_exp_f32_e32 v72, v90
	v_exp_f32_e32 v73, v91
	v_pk_fma_f32 v[80:81], v[74:75], v[60:61], v[80:81] op_sel_hi:[0,1,1] neg_lo:[1,0,0] neg_hi:[1,0,0]
	v_pk_fma_f32 v[82:83], v[74:75], v[62:63], v[82:83] op_sel_hi:[0,1,1] neg_lo:[1,0,0] neg_hi:[1,0,0]
	v_pk_fma_f32 v[84:85], v[74:75], v[64:65], v[84:85] op_sel:[1,0,0] neg_lo:[1,0,0] neg_hi:[1,0,0]
	v_pk_fma_f32 v[86:87], v[74:75], v[66:67], v[86:87] op_sel:[1,0,0] neg_lo:[1,0,0] neg_hi:[1,0,0]
	s_waitcnt lgkmcnt(0)
	ds_read2_b32 v[40:41], v92 offset0:16 offset1:168
	ds_read2_b32 v[42:43], v93 offset0:16 offset1:168
	ds_read2_b32 v[44:45], v94 offset0:16 offset1:168
	ds_read2_b32 v[46:47], v95 offset0:16 offset1:168
	ds_read2_b32 v[48:49], v96 offset0:16 offset1:168
	v_pk_add_f32 v[88:89], v[88:89], v[58:59]
	v_pk_add_f32 v[74:75], v[58:59], v[58:59]
	v_pk_fma_f32 v[60:61], v[72:73], v[50:51], v[124:125] op_sel_hi:[0,1,1]
	v_pk_fma_f32 v[62:63], v[72:73], v[52:53], v[124:125] op_sel_hi:[0,1,1]
	v_pk_fma_f32 v[64:65], v[72:73], v[54:55], v[124:125] op_sel:[1,0,0]
	v_pk_fma_f32 v[66:67], v[72:73], v[56:57], v[124:125] op_sel:[1,0,0]
	v_rcp_f32_e32 v60, v60
	v_rcp_f32_e32 v61, v61
	v_rcp_f32_e32 v62, v62
	v_rcp_f32_e32 v63, v63
	v_rcp_f32_e32 v64, v64
	v_rcp_f32_e32 v65, v65
	v_rcp_f32_e32 v66, v66
	v_rcp_f32_e32 v67, v67
	s_waitcnt vmcnt(4)
	v_pk_mul_f32 v[90:91], v[34:35], v[126:127]
	s_nop 0
	v_med3_f32 v90, v90, s0, v97
	v_med3_f32 v91, v91, s0, v97
	v_exp_f32_e32 v68, v90
	v_exp_f32_e32 v69, v91
	v_pk_fma_f32 v[80:81], v[74:75], v[60:61], v[80:81] op_sel_hi:[0,1,1] neg_lo:[1,0,0] neg_hi:[1,0,0]
	v_pk_fma_f32 v[82:83], v[74:75], v[62:63], v[82:83] op_sel_hi:[0,1,1] neg_lo:[1,0,0] neg_hi:[1,0,0]
	v_pk_fma_f32 v[84:85], v[74:75], v[64:65], v[84:85] op_sel:[1,0,0] neg_lo:[1,0,0] neg_hi:[1,0,0]
	v_pk_fma_f32 v[86:87], v[74:75], v[66:67], v[86:87] op_sel:[1,0,0] neg_lo:[1,0,0] neg_hi:[1,0,0]
	s_waitcnt lgkmcnt(0)
	ds_read2_b32 v[50:51], v92 offset0:17 offset1:169
	ds_read2_b32 v[52:53], v93 offset0:17 offset1:169
	ds_read2_b32 v[54:55], v94 offset0:17 offset1:169
	ds_read2_b32 v[56:57], v95 offset0:17 offset1:169
	ds_read2_b32 v[58:59], v96 offset0:17 offset1:169
	v_pk_add_f32 v[88:89], v[88:89], v[48:49]
	v_pk_add_f32 v[74:75], v[48:49], v[48:49]
	v_pk_fma_f32 v[60:61], v[68:69], v[40:41], v[124:125] op_sel_hi:[0,1,1]
	v_pk_fma_f32 v[62:63], v[68:69], v[42:43], v[124:125] op_sel_hi:[0,1,1]
	v_pk_fma_f32 v[64:65], v[68:69], v[44:45], v[124:125] op_sel:[1,0,0]
	v_pk_fma_f32 v[66:67], v[68:69], v[46:47], v[124:125] op_sel:[1,0,0]
	v_rcp_f32_e32 v60, v60
	v_rcp_f32_e32 v61, v61
	v_rcp_f32_e32 v62, v62
	v_rcp_f32_e32 v63, v63
	v_rcp_f32_e32 v64, v64
	v_rcp_f32_e32 v65, v65
	v_rcp_f32_e32 v66, v66
	v_rcp_f32_e32 v67, v67
	s_waitcnt vmcnt(2)
	v_pk_mul_f32 v[90:91], v[36:37], v[126:127]
	s_nop 0
	v_med3_f32 v90, v90, s0, v97
	v_med3_f32 v91, v91, s0, v97
	v_exp_f32_e32 v72, v90
	v_exp_f32_e32 v73, v91
	v_pk_fma_f32 v[80:81], v[74:75], v[60:61], v[80:81] op_sel_hi:[0,1,1] neg_lo:[1,0,0] neg_hi:[1,0,0]
	v_pk_fma_f32 v[82:83], v[74:75], v[62:63], v[82:83] op_sel_hi:[0,1,1] neg_lo:[1,0,0] neg_hi:[1,0,0]
	v_pk_fma_f32 v[84:85], v[74:75], v[64:65], v[84:85] op_sel:[1,0,0] neg_lo:[1,0,0] neg_hi:[1,0,0]
	v_pk_fma_f32 v[86:87], v[74:75], v[66:67], v[86:87] op_sel:[1,0,0] neg_lo:[1,0,0] neg_hi:[1,0,0]
	s_waitcnt lgkmcnt(0)
	ds_read2_b32 v[40:41], v92 offset0:18 offset1:170
	ds_read2_b32 v[42:43], v93 offset0:18 offset1:170
	ds_read2_b32 v[44:45], v94 offset0:18 offset1:170
	ds_read2_b32 v[46:47], v95 offset0:18 offset1:170
	ds_read2_b32 v[48:49], v96 offset0:18 offset1:170
	v_pk_add_f32 v[88:89], v[88:89], v[58:59]
	v_pk_add_f32 v[74:75], v[58:59], v[58:59]
	v_pk_fma_f32 v[60:61], v[72:73], v[50:51], v[124:125] op_sel_hi:[0,1,1]
	v_pk_fma_f32 v[62:63], v[72:73], v[52:53], v[124:125] op_sel_hi:[0,1,1]
	v_pk_fma_f32 v[64:65], v[72:73], v[54:55], v[124:125] op_sel:[1,0,0]
	v_pk_fma_f32 v[66:67], v[72:73], v[56:57], v[124:125] op_sel:[1,0,0]
	v_rcp_f32_e32 v60, v60
	v_rcp_f32_e32 v61, v61
	v_rcp_f32_e32 v62, v62
	v_rcp_f32_e32 v63, v63
	v_rcp_f32_e32 v64, v64
	v_rcp_f32_e32 v65, v65
	v_rcp_f32_e32 v66, v66
	v_rcp_f32_e32 v67, v67
	s_waitcnt vmcnt(0)
	v_pk_mul_f32 v[90:91], v[118:119], v[126:127]
	s_nop 0
	v_med3_f32 v90, v90, s0, v97
	v_med3_f32 v91, v91, s0, v97
	v_exp_f32_e32 v68, v90
	v_exp_f32_e32 v69, v91
	v_pk_fma_f32 v[80:81], v[74:75], v[60:61], v[80:81] op_sel_hi:[0,1,1] neg_lo:[1,0,0] neg_hi:[1,0,0]
	v_pk_fma_f32 v[82:83], v[74:75], v[62:63], v[82:83] op_sel_hi:[0,1,1] neg_lo:[1,0,0] neg_hi:[1,0,0]
	v_pk_fma_f32 v[84:85], v[74:75], v[64:65], v[84:85] op_sel:[1,0,0] neg_lo:[1,0,0] neg_hi:[1,0,0]
	v_pk_fma_f32 v[86:87], v[74:75], v[66:67], v[86:87] op_sel:[1,0,0] neg_lo:[1,0,0] neg_hi:[1,0,0]
	s_waitcnt lgkmcnt(0)
	v_pk_add_f32 v[88:89], v[88:89], v[48:49]
	v_pk_add_f32 v[74:75], v[48:49], v[48:49]
	v_pk_fma_f32 v[60:61], v[68:69], v[40:41], v[124:125] op_sel_hi:[0,1,1]
	v_pk_fma_f32 v[62:63], v[68:69], v[42:43], v[124:125] op_sel_hi:[0,1,1]
	v_pk_fma_f32 v[64:65], v[68:69], v[44:45], v[124:125] op_sel:[1,0,0]
	v_pk_fma_f32 v[66:67], v[68:69], v[46:47], v[124:125] op_sel:[1,0,0]
	v_rcp_f32_e32 v60, v60
	v_rcp_f32_e32 v61, v61
	v_rcp_f32_e32 v62, v62
	v_rcp_f32_e32 v63, v63
	v_rcp_f32_e32 v64, v64
	v_rcp_f32_e32 v65, v65
	v_rcp_f32_e32 v66, v66
	v_rcp_f32_e32 v67, v67
	s_nop 0
	v_pk_fma_f32 v[80:81], v[74:75], v[60:61], v[80:81] op_sel_hi:[0,1,1] neg_lo:[1,0,0] neg_hi:[1,0,0]
	v_pk_fma_f32 v[82:83], v[74:75], v[62:63], v[82:83] op_sel_hi:[0,1,1] neg_lo:[1,0,0] neg_hi:[1,0,0]
	v_pk_fma_f32 v[84:85], v[74:75], v[64:65], v[84:85] op_sel:[1,0,0] neg_lo:[1,0,0] neg_hi:[1,0,0]
	v_pk_fma_f32 v[86:87], v[74:75], v[66:67], v[86:87] op_sel:[1,0,0] neg_lo:[1,0,0] neg_hi:[1,0,0]
	v_add_f32_e32 v80, v88, v80
	v_add_f32_e32 v81, v88, v81
	v_add_f32_e32 v82, v88, v82
	v_add_f32_e32 v83, v88, v83
	v_add_f32_e32 v84, v89, v84
	v_add_f32_e32 v85, v89, v85
	v_add_f32_e32 v86, v89, v86
	v_add_f32_e32 v87, v89, v87
	v_add_f32_e32 v76, v76, v77
	v_add_f32_e32 v78, v78, v79
	v_add_f32_e32 v120, v120, v121
	v_add_f32_e32 v122, v122, v123
	v_mul_u32_u24_e32 v6, 0x1800, v1
	v_or_b32_e32 v6, v38, v6
	ds_write2st64_b32 v6, v80, v81 offset1:2
	ds_write2st64_b32 v6, v82, v83 offset0:4 offset1:6
	ds_write2st64_b32 v6, v76, v78 offset0:8 offset1:10
	ds_write2st64_b32 v6, v120, v122 offset0:12 offset1:14
	ds_write2st64_b32 v6, v84, v85 offset0:16 offset1:18
	ds_write2st64_b32 v6, v86, v87 offset0:20 offset1:22
	v_or_b32_e32 v10, 0xc000, v38
	v_lshl_or_b32 v11, v1, 9, v38
	v_add_u32_e32 v1, 4, v1
	v_mov_b32_e32 v12, v0
	s_mov_b64 s[4:5], 0
	s_movk_i32 s8, 0x1ff
	s_movk_i32 s9, 0x3ff
	s_waitcnt lgkmcnt(0)
	s_barrier
	s_branch .LBB2_21
